# strategy 7.4 other half: static s_setprio 1 for waves 0-3 during the attention phases
# baseline (speedup 1.0000x reference)
.LBB0_720:
	v_readlane_b32 s0, v254, 60
	s_add_i32 s2, s0, 4
	v_readlane_b32 s4, v253, 4
	v_readlane_b32 s5, v253, 5
	s_cmp_gt_i32 s4, s2
	s_cselect_b64 s[0:1], -1, 0
	s_cmp_ge_i32 s2, s5
	s_cselect_b64 s[2:3], -1, 0
	s_or_b64 s[0:1], s[0:1], s[2:3]
	s_and_b64 vcc, exec, s[0:1]
	v_readlane_b32 s6, v253, 6
	v_readlane_b32 s7, v253, 7
	s_cbranch_vccnz .LBB0_1097
	s_cmp_lt_u32 s56, 4
	s_cbranch_scc0 .Lattn_prio_done
	s_setprio 1
